# stack14
# speedup vs baseline: 1.0173x; 1.0044x over previous
.LBB3_51:
	v_max3_f32 v74, |v182|, 0, |v183|
	v_max3_f32 v74, v74, |v184|, |v185|
	v_max3_f32 v74, v74, |v186|, |v187|
	v_max3_f32 v74, v74, |v188|, |v189|
	v_max3_f32 v74, v74, |v198|, |v199|
	v_max3_f32 v74, v74, |v200|, |v201|
	v_max3_f32 v74, v74, |v202|, |v203|
	v_max3_f32 v74, v74, |v204|, |v205|
	v_max3_f32 v74, v74, |v214|, |v215|
	v_max3_f32 v74, v74, |v216|, |v217|
	v_max3_f32 v74, v74, |v218|, |v219|
	v_max3_f32 v74, v74, |v220|, |v221|
	v_max3_f32 v74, v74, |v222|, |v223|
	v_max3_f32 v74, v74, |v224|, |v225|
	v_max3_f32 v74, v74, |v226|, |v227|
	s_waitcnt vmcnt(0)
	v_max3_f32 v74, v74, |v228|, |v229|
	ds_read_u16 v62, v233 offset:4096
	v_pk_fma_f32 v[66:67], v[230:231], v[206:207], v[162:163] neg_lo:[0,0,1] neg_hi:[0,0,1]
	v_pk_fma_f32 v[68:69], v[230:231], v[208:209], v[160:161] neg_lo:[0,0,1] neg_hi:[0,0,1]
	v_max3_f32 v58, v74, |v66|, |v67|
	v_pk_fma_f32 v[70:71], v[230:231], v[210:211], v[158:159] neg_lo:[0,0,1] neg_hi:[0,0,1]
	v_max3_f32 v58, v58, |v68|, |v69|
	v_pk_fma_f32 v[72:73], v[230:231], v[212:213], v[156:157] neg_lo:[0,0,1] neg_hi:[0,0,1]
	v_max3_f32 v58, v58, |v70|, |v71|
	v_max3_f32 v63, v58, |v72|, |v73|
	v_fma_mixlo_f16 v58, v66, v164, 0 op_sel_hi:[0,0,0]
	v_fma_mixlo_f16 v59, v68, v164, 0 op_sel_hi:[0,0,0]
	v_fma_mixlo_f16 v60, v70, v164, 0 op_sel_hi:[0,0,0]
	v_fma_mixlo_f16 v61, v72, v164, 0 op_sel_hi:[0,0,0]
	s_waitcnt lgkmcnt(0)
	v_lshl_add_u32 v62, v62, 4, s67
	v_fma_mixhi_f16 v58, v67, v164, 0 op_sel_hi:[0,0,0]
	v_fma_mixhi_f16 v59, v69, v164, 0 op_sel_hi:[0,0,0]
	v_fma_mixhi_f16 v60, v71, v164, 0 op_sel_hi:[0,0,0]
	v_fma_mixhi_f16 v61, v73, v164, 0 op_sel_hi:[0,0,0]
	ds_write_b128 v62, v[58:61]
	v_pk_fma_f32 v[74:75], v[230:231], v[190:191], v[146:147] neg_lo:[0,0,1] neg_hi:[0,0,1]
	ds_read_u16 v62, v233 offset:5120
	v_pk_fma_f32 v[76:77], v[230:231], v[192:193], v[144:145] neg_lo:[0,0,1] neg_hi:[0,0,1]
	v_max3_f32 v58, v63, |v74|, |v75|
	v_pk_fma_f32 v[78:79], v[230:231], v[194:195], v[142:143] neg_lo:[0,0,1] neg_hi:[0,0,1]
	v_max3_f32 v58, v58, |v76|, |v77|
	v_pk_fma_f32 v[80:81], v[230:231], v[196:197], v[140:141] neg_lo:[0,0,1] neg_hi:[0,0,1]
	v_max3_f32 v58, v58, |v78|, |v79|
	v_max3_f32 v63, v58, |v80|, |v81|
	v_fma_mixlo_f16 v58, v74, v164, 0 op_sel_hi:[0,0,0]
	v_fma_mixhi_f16 v58, v75, v164, 0 op_sel_hi:[0,0,0]
	v_fma_mixlo_f16 v59, v76, v164, 0 op_sel_hi:[0,0,0]
	v_fma_mixlo_f16 v60, v78, v164, 0 op_sel_hi:[0,0,0]
	v_fma_mixlo_f16 v61, v80, v164, 0 op_sel_hi:[0,0,0]
	s_waitcnt lgkmcnt(0)
	v_lshl_add_u32 v62, v62, 4, s67
	v_pk_fma_f32 v[82:83], v[230:231], v[174:175], v[138:139] neg_lo:[0,0,1] neg_hi:[0,0,1]
	v_fma_mixhi_f16 v59, v77, v164, 0 op_sel_hi:[0,0,0]
	v_fma_mixhi_f16 v60, v79, v164, 0 op_sel_hi:[0,0,0]
	v_fma_mixhi_f16 v61, v81, v164, 0 op_sel_hi:[0,0,0]
	ds_write_b128 v62, v[58:61]
	v_pk_fma_f32 v[84:85], v[230:231], v[176:177], v[136:137] neg_lo:[0,0,1] neg_hi:[0,0,1]
	v_max3_f32 v58, v63, |v82|, |v83|
	v_pk_fma_f32 v[86:87], v[230:231], v[178:179], v[134:135] neg_lo:[0,0,1] neg_hi:[0,0,1]
	v_max3_f32 v58, v58, |v84|, |v85|
	v_pk_fma_f32 v[88:89], v[230:231], v[180:181], v[132:133] neg_lo:[0,0,1] neg_hi:[0,0,1]
	v_max3_f32 v58, v58, |v86|, |v87|
	v_max3_f32 v92, v58, |v88|, |v89|
	v_pk_fma_f32 v[62:63], v[230:231], v[166:167], v[148:149] neg_lo:[0,0,1] neg_hi:[0,0,1]
	v_pk_fma_f32 v[64:65], v[230:231], v[168:169], v[150:151] neg_lo:[0,0,1] neg_hi:[0,0,1]
	v_max3_f32 v92, v92, |v62|, |v63|
	v_pk_fma_f32 v[58:59], v[230:231], v[170:171], v[152:153] neg_lo:[0,0,1] neg_hi:[0,0,1]
	v_max3_f32 v92, v92, |v64|, |v65|
	v_pk_fma_f32 v[60:61], v[230:231], v[172:173], v[154:155] neg_lo:[0,0,1] neg_hi:[0,0,1]
	v_max3_f32 v92, v92, |v58|, |v59|
	v_max3_f32 v93, v92, |v60|, |v61|
	v_mov_b32_e32 v95, v93
	ds_read_u16 v94, v233 offset:6144
	ds_read_u16 v97, v233 offset:7168
	v_max_f32_dpp v95, v95, v95 row_shr:1 row_mask:0xf bank_mask:0xf
	v_fma_mixlo_f16 v90, v82, v164, 0 op_sel_hi:[0,0,0]
	v_fma_mixlo_f16 v91, v84, v164, 0 op_sel_hi:[0,0,0]
	v_max_f32_dpp v95, v95, v95 row_shr:2 row_mask:0xf bank_mask:0xf
	v_fma_mixlo_f16 v92, v86, v164, 0 op_sel_hi:[0,0,0]
	v_fma_mixlo_f16 v93, v88, v164, 0 op_sel_hi:[0,0,0]
	v_max_f32_dpp v95, v95, v95 row_shr:4 row_mask:0xf bank_mask:0xf
	v_fma_mixhi_f16 v90, v83, v164, 0 op_sel_hi:[0,0,0]
	v_fma_mixhi_f16 v91, v85, v164, 0 op_sel_hi:[0,0,0]
	v_max_f32_dpp v95, v95, v95 row_shr:8 row_mask:0xf bank_mask:0xf
	v_fma_mixhi_f16 v92, v87, v164, 0 op_sel_hi:[0,0,0]
	v_fma_mixhi_f16 v93, v89, v164, 0 op_sel_hi:[0,0,0]
	v_fma_mixlo_f16 v98, v62, v164, 0 op_sel_hi:[0,0,0]
	v_fma_mixlo_f16 v99, v64, v164, 0 op_sel_hi:[0,0,0]
	v_fma_mixlo_f16 v100, v58, v164, 0 op_sel_hi:[0,0,0]
	v_fma_mixlo_f16 v101, v60, v164, 0 op_sel_hi:[0,0,0]
	s_waitcnt lgkmcnt(0)
	v_lshl_add_u32 v94, v94, 4, s67
	v_lshl_add_u32 v96, v97, 4, s67
	v_fma_mixhi_f16 v98, v63, v164, 0 op_sel_hi:[0,0,0]
	v_fma_mixhi_f16 v99, v65, v164, 0 op_sel_hi:[0,0,0]
	v_fma_mixhi_f16 v100, v59, v164, 0 op_sel_hi:[0,0,0]
	v_fma_mixhi_f16 v101, v61, v164, 0 op_sel_hi:[0,0,0]
	ds_write_b128 v94, v[90:93]
	ds_write_b128 v96, v[98:101]
	s_lshl_b32 s19, s34, 2
	s_add_i32 s19, s19, 0x22000
	v_mov_b32_e32 v90, s19
	s_mov_b32 s24, 0x80008000
	s_mov_b32 s25, 0x80008000
	s_mov_b64 exec, s[24:25]
	ds_max_u32 v90, v95
	s_mov_b64 exec, -1
	s_mov_b64 s[24:25], -1
